# c9
# speedup vs baseline: 1.0135x; 1.0003x over previous
.LBB6_525:
	s_or_b64 exec, exec, s[10:11]
	v_mov_b32_e32 v33, v24
	v_mov_b32_e32 v24, v25
	v_mov_b32_e32 v25, v26
	v_pk_add_f32 v[184:185], v[68:69], v[24:25]
	v_mov_b32_e32 v24, v82
	v_mov_b32_e32 v25, v70
	v_mov_b32_e32 v26, v55
	v_pk_add_f32 v[180:181], v[24:25], v[26:27]
	v_mov_b32_e32 v24, v83
	v_mov_b32_e32 v25, v84
	v_mov_b32_e32 v32, v23
	v_pk_add_f32 v[186:187], v[24:25], v[56:57]
	v_mov_b32_e32 v24, v85
	v_mov_b32_e32 v25, v86
	v_pk_add_f32 v[182:183], v[66:67], v[32:33]
	v_pk_add_f32 v[188:189], v[24:25], v[58:59]
	s_waitcnt lgkmcnt(1)
	v_mfma_f32_32x32x16_f16 v[2:17], v[116:119], v[60:63], v[2:17]
	s_waitcnt lgkmcnt(0)
	v_mfma_f32_32x32x16_f16 v[2:17], v[112:115], v[28:31], v[2:17]
	s_add_i32 s3, s3, s33
	s_bfe_u32 s3, s3, 0x30003
	s_lshl_b32 s10, s3, 17
	s_lshl_b32 s2, s2, 9
	s_add_i32 s10, s40, s10
	s_and_b32 s2, s2, 0x7000
	s_add_i32 s2, s2, s10
	s_nop 4
	v_lshl_add_u32 v17, v200, 15, s2
	v_add_lshl_u32 v23, v201, v191, 10
	s_movk_i32 s10, 0xfc80
	v_add3_u32 v193, v17, v23, s10
	v_lshl_add_u32 v17, v198, 15, s2
	v_add_lshl_u32 v23, v199, v197, 10
	s_mov_b32 s10, 0xffff7c80
	v_add3_u32 v216, v17, v23, s10
	v_lshl_add_u32 v17, v195, 15, s2
	v_add_lshl_u32 v23, v196, v191, 10
	v_add3_u32 v217, v17, v23, s10
	s_lshl_b32 s2, s3, 7
	v_lshlrev_b32_e32 v17, 5, v194
	v_or3_b32 v17, v190, s2, v17
	v_add_u32_e32 v17, s41, v17
	v_add_lshl_u32 v17, v17, v202, 10
	v_add3_u32 v32, s40, v17, v206
	v_mov_b32_e32 v33, 0
	v_add_u32_e32 v17, 32, v32
	v_lshlrev_b64 v[194:195], 4, v[32:33]
	v_lshl_add_u64 v[24:25], v[32:33], 2, s[18:19]
	s_mov_b64 s[10:11], 0x100
	v_lshlrev_b32_e32 v32, 2, v17
	s_mov_b32 s33, 2
	v_lshl_add_u64 v[196:197], v[24:25], 0, s[10:11]
	v_lshl_add_u64 v[198:199], s[18:19], 0, v[32:33]
	v_lshlrev_b32_e32 v200, 4, v17
	v_mov_b32_e32 v201, v33
	v_mbcnt_lo_u32_b32 v24, -1, 0
	v_mbcnt_hi_u32_b32 v24, -1, v24
	v_and_b32_e32 v24, 31, v24
	v_cmp_eq_u32_e64 s[70:71], 0, v24
	v_cmp_eq_u32_e64 s[72:73], 31, v24
	v_mul_u32_u24_e32 v25, 11, v24
	v_lshrrev_b32_e32 v25, 5, v25
	v_mul_u32_u24_e32 v25, 3, v25
	v_sub_u32_e32 v24, v24, v25
	v_mul_u32_u24_e32 v26, 12, v24
	v_cndmask_b32_e64 v26, v26, 12, s[70:71]
	v_add_u32_e32 v25, 2, v24
	v_mul_u32_u24_e32 v27, 11, v25
	v_lshrrev_b32_e32 v27, 5, v27
	v_mul_u32_u24_e32 v27, 3, v27
	v_sub_u32_e32 v25, v25, v27
	v_mul_u32_u24_e32 v25, 12, v25
	v_add_u32_e32 v25, -12, v25
	v_add_u32_e32 v24, 1, v24
	v_mul_u32_u24_e32 v27, 11, v24
	v_lshrrev_b32_e32 v27, 5, v27
	v_mul_u32_u24_e32 v27, 3, v27
	v_sub_u32_e32 v24, v24, v27
	v_mul_u32_u24_e32 v24, 12, v24
	v_add_u32_e32 v24, 0xffffffe8, v24
	v_cndmask_b32_e64 v24, v24, -12, s[72:73]
	v_add_u32_e32 v230, v212, v25
	v_add_u32_e32 v231, v212, v26
	v_add_u32_e32 v232, v212, v24
	v_add_u32_e32 v233, v214, v25
	v_add_u32_e32 v234, v214, v26
	v_add_u32_e32 v235, v214, v24
	v_add_u32_e32 v236, v215, v25
	v_add_u32_e32 v237, v215, v26
	v_add_u32_e32 v238, v215, v24
	s_nop 0
	s_nop 0
	s_barrier
